# v78 plus nt on the final output stores and read-once row loads of P15 and on the read-once adaLN weight loads of P0
# speedup vs baseline: 1.0076x; 1.0055x over previous
; __device__ __forceinline__ void p0_prologue(Frame& F, const Args& a) {
;     ...
;     for (int item = blockIdx.x; item < 2 * (NMOD / 16); item += F.G) {
;         const int l = item / (NMOD / 16), n0 = (item % (NMOD / 16)) * 16, col = lane & 15, kpar = lane >> 4;
;         const float* wp = w_ada + (size_t)l * D * NMOD + n0 + col;
;         float a0 = 0.f, a1 = 0.f, a2 = 0.f, a3 = 0.f;
; #pragma unroll 16
;         for (int i = 0; i < 32; ++i) { const int k = 128 * F.wave + 4 * i + kpar; const float wv = wp[(size_t)k * NMOD];
;             a0 += sc[k] * wv; a1 += sc[D + k] * wv; a2 += sc[2 * D + k] * wv; a3 += sc[3 * D + k] * wv; }
;         a0 += __shfl_xor(a0, 16); a1 += __shfl_xor(a1, 16); a2 += __shfl_xor(a2, 16); a3 += __shfl_xor(a3, 16);
.LBB0_19:
	v_subrev_u32_e32 v21, 60, v19
	v_subrev_u32_e32 v24, 56, v19
	v_subrev_u32_e32 v26, 52, v19
	v_subrev_u32_e32 v28, 48, v19
	v_subrev_u32_e32 v30, 44, v19
	v_mad_i64_i32 v[12:13], s[16:17], v19, s3, v[6:7]
	v_mad_i64_i32 v[22:23], s[16:17], v21, s3, v[6:7]
	v_mad_i64_i32 v[24:25], s[16:17], v24, s3, v[6:7]
	v_mad_i64_i32 v[26:27], s[16:17], v26, s3, v[6:7]
	v_mad_i64_i32 v[28:29], s[16:17], v28, s3, v[6:7]
	v_mad_i64_i32 v[30:31], s[16:17], v30, s3, v[6:7]
	global_load_dword v12, v[12:13], off nt
	s_nop 0
	global_load_dword v22, v[22:23], off nt
	s_nop 0
	global_load_dword v24, v[24:25], off nt
	s_nop 0
	global_load_dword v26, v[26:27], off nt
	s_nop 0
	global_load_dword v28, v[28:29], off nt
	s_nop 0
	global_load_dword v30, v[30:31], off nt
	v_add_u32_e32 v20, s12, v17
	v_subrev_u32_e32 v32, 40, v19
	v_subrev_u32_e32 v34, 36, v19
	v_subrev_u32_e32 v36, 32, v19
	v_subrev_u32_e32 v38, 28, v19
	v_add_u32_e32 v50, -4, v19
	v_add_u32_e32 v51, 0x18000, v20
	v_add_u32_e32 v52, 0x19000, v20
	v_add_u32_e32 v53, 0x1a000, v20
	v_mad_i64_i32 v[32:33], s[16:17], v32, s3, v[6:7]
	v_mad_i64_i32 v[34:35], s[16:17], v34, s3, v[6:7]
	v_mad_i64_i32 v[36:37], s[16:17], v36, s3, v[6:7]
	v_mad_i64_i32 v[38:39], s[16:17], v38, s3, v[6:7]
	v_add_u32_e32 v54, 0x1b000, v20
	v_add_u32_e32 v55, 0x18010, v20
	v_add_u32_e32 v56, 0x19010, v20
	v_add_u32_e32 v57, 0x1a010, v20
	v_add_u32_e32 v58, 0x1b010, v20
	v_add_u32_e32 v59, 0x18020, v20
	v_add_u32_e32 v60, 0x19020, v20
	v_add_u32_e32 v61, 0x1a020, v20
	v_add_u32_e32 v62, 0x1b020, v20
	v_add_u32_e32 v63, 0x18030, v20
	v_add_u32_e32 v64, 0x19030, v20
	v_add_u32_e32 v65, 0x1a030, v20
	v_add_u32_e32 v66, 0x1b030, v20
	v_add_u32_e32 v67, 0x18040, v20
	v_add_u32_e32 v68, 0x19040, v20
	v_add_u32_e32 v69, 0x1a040, v20
	v_add_u32_e32 v70, 0x1b040, v20
	v_add_u32_e32 v71, 0x18050, v20
	v_add_u32_e32 v72, 0x19050, v20
	v_add_u32_e32 v73, 0x1a050, v20
	v_add_u32_e32 v74, 0x1b050, v20
	v_add_u32_e32 v75, 0x18060, v20
	v_add_u32_e32 v76, 0x19060, v20
	v_add_u32_e32 v77, 0x1a060, v20
	v_add_u32_e32 v78, 0x1b060, v20
	v_add_u32_e32 v79, 0x18070, v20
	v_add_u32_e32 v80, 0x19070, v20
	v_add_u32_e32 v81, 0x1a070, v20
	v_add_u32_e32 v82, 0x1b070, v20
	v_add_u32_e32 v83, 0x18080, v20
	v_add_u32_e32 v84, 0x19080, v20
	v_add_u32_e32 v85, 0x1a080, v20
	v_add_u32_e32 v86, 0x1b080, v20
	v_add_u32_e32 v87, 0x18090, v20
	v_add_u32_e32 v88, 0x19090, v20
	v_add_u32_e32 v89, 0x1a090, v20
	v_add_u32_e32 v90, 0x1b090, v20
	v_add_u32_e32 v91, 0x180a0, v20
	v_add_u32_e32 v92, 0x190a0, v20
	v_add_u32_e32 v93, 0x1a0a0, v20
	v_add_u32_e32 v94, 0x1b0a0, v20
	v_add_u32_e32 v95, 0x180b0, v20
	v_add_u32_e32 v96, 0x190b0, v20
	v_add_u32_e32 v97, 0x1a0b0, v20
	v_add_u32_e32 v98, 0x1b0b0, v20
	v_add_u32_e32 v99, 0x180c0, v20
	v_add_u32_e32 v100, 0x190c0, v20
	v_add_u32_e32 v101, 0x1a0c0, v20
	v_add_u32_e32 v102, 0x1b0c0, v20
	v_add_u32_e32 v103, 0x180d0, v20
	v_add_u32_e32 v104, 0x190d0, v20
	v_add_u32_e32 v105, 0x1a0d0, v20
	v_add_u32_e32 v106, 0x1b0d0, v20
	v_add_u32_e32 v107, 0x180e0, v20
	v_add_u32_e32 v108, 0x190e0, v20
	v_add_u32_e32 v109, 0x1a0e0, v20
	v_add_u32_e32 v110, 0x1b0e0, v20
	v_add_u32_e32 v111, 0x180f0, v20
	v_add_u32_e32 v112, 0x190f0, v20
	v_add_u32_e32 v113, 0x1a0f0, v20
	v_add_u32_e32 v114, 0x1b0f0, v20
	v_mad_i64_i32 v[20:21], s[16:17], v50, s3, v[6:7]
	ds_read_b32 v50, v51
	ds_read_b32 v51, v52
	ds_read_b32 v52, v53
	ds_read_b32 v53, v54
	global_load_dword v32, v[32:33], off nt
	s_nop 0
	global_load_dword v34, v[34:35], off nt
	s_nop 0
	global_load_dword v36, v[36:37], off nt
	s_nop 0
	global_load_dword v38, v[38:39], off nt
	v_subrev_u32_e32 v40, 24, v19
	v_subrev_u32_e32 v42, 20, v19
	v_add_u32_e32 v44, -16, v19
	v_add_u32_e32 v46, -12, v19
	v_mad_i64_i32 v[40:41], s[16:17], v40, s3, v[6:7]
	v_mad_i64_i32 v[42:43], s[16:17], v42, s3, v[6:7]
	v_mad_i64_i32 v[44:45], s[16:17], v44, s3, v[6:7]
	v_mad_i64_i32 v[46:47], s[16:17], v46, s3, v[6:7]
	v_add_u32_e32 v48, -8, v19
	ds_read_b32 v54, v55
	ds_read_b32 v55, v56
	ds_read_b32 v56, v57
	ds_read_b32 v57, v58
	global_load_dword v40, v[40:41], off nt
	s_nop 0
	global_load_dword v42, v[42:43], off nt
	s_nop 0
	global_load_dword v44, v[44:45], off nt
	s_nop 0
	global_load_dword v46, v[46:47], off nt
	v_mad_i64_i32 v[48:49], s[16:17], v48, s3, v[6:7]
	ds_read_b32 v58, v59
	ds_read_b32 v59, v60
	ds_read_b32 v60, v61
	ds_read_b32 v61, v62
	global_load_dword v48, v[48:49], off nt
	s_nop 0
	global_load_dword v20, v[20:21], off nt
	s_waitcnt vmcnt(14) lgkmcnt(10)
	v_pk_fma_f32 v[8:9], v[22:23], v[50:51], v[8:9] op_sel_hi:[0,1,1]
	s_waitcnt lgkmcnt(8)
; __device__ __forceinline__ void p0_prologue(Frame& F, const Args& a) {
;     ...
; #pragma unroll 16
;         for (int i = 0; i < 32; ++i) { const int k = 128 * F.wave + 4 * i + kpar; const float wv = wp[(size_t)k * NMOD];
;             a0 += sc[k] * wv; a1 += sc[D + k] * wv; a2 += sc[2 * D + k] * wv; a3 += sc[3 * D + k] * wv; }
;         a0 += __shfl_xor(a0, 16); a1 += __shfl_xor(a1, 16); a2 += __shfl_xor(a2, 16); a3 += __shfl_xor(a3, 16);
;         a0 += __shfl_xor(a0, 32); a1 += __shfl_xor(a1, 32); a2 += __shfl_xor(a2, 32); a3 += __shfl_xor(a3, 32);
;         if (lane < 16) { red[(F.wave * 4 + 0) * 16 + col] = a0; red[(F.wave * 4 + 1) * 16 + col] = a1; red[(F.wave * 4 + 2) * 16 + col] = a2; red[(F.wave * 4 + 3) * 16 + col] = a3; }
	v_pk_fma_f32 v[10:11], v[22:23], v[52:53], v[10:11] op_sel_hi:[0,1,1]
	s_waitcnt vmcnt(13) lgkmcnt(6)
	v_pk_fma_f32 v[8:9], v[24:25], v[54:55], v[8:9] op_sel_hi:[0,1,1]
	s_waitcnt lgkmcnt(4)
	v_pk_fma_f32 v[10:11], v[24:25], v[56:57], v[10:11] op_sel_hi:[0,1,1]
	s_waitcnt vmcnt(12) lgkmcnt(2)
	v_pk_fma_f32 v[8:9], v[26:27], v[58:59], v[8:9] op_sel_hi:[0,1,1]
	s_waitcnt lgkmcnt(0)
	v_pk_fma_f32 v[10:11], v[26:27], v[60:61], v[10:11] op_sel_hi:[0,1,1]
	ds_read_b32 v62, v63
	ds_read_b32 v63, v64
	ds_read_b32 v64, v65
	ds_read_b32 v65, v66
	ds_read_b32 v66, v67
	ds_read_b32 v67, v68
	ds_read_b32 v68, v69
	ds_read_b32 v69, v70
	ds_read_b32 v70, v71
	ds_read_b32 v71, v72
	ds_read_b32 v72, v73
	ds_read_b32 v73, v74
	ds_read_b32 v74, v75
	ds_read_b32 v75, v76
	ds_read_b32 v76, v77
	ds_read_b32 v77, v78
	ds_read_b32 v78, v79
	ds_read_b32 v79, v80
	ds_read_b32 v80, v81
	ds_read_b32 v81, v82
	ds_read_b32 v82, v83
	ds_read_b32 v83, v84
	ds_read_b32 v84, v85
	ds_read_b32 v85, v86
	ds_read_b32 v86, v87
	ds_read_b32 v87, v88
	ds_read_b32 v88, v89
	ds_read_b32 v89, v90
	ds_read_b32 v90, v91
	ds_read_b32 v91, v92
	ds_read_b32 v92, v93
	ds_read_b32 v93, v94
	ds_read_b32 v94, v95
	ds_read_b32 v95, v96
	ds_read_b32 v96, v97
	ds_read_b32 v97, v98
	ds_read_b32 v98, v99
	ds_read_b32 v99, v100
	ds_read_b32 v100, v101
	ds_read_b32 v101, v102
	ds_read_b32 v102, v103
	ds_read_b32 v103, v104
	ds_read_b32 v104, v105
	ds_read_b32 v105, v106
	ds_read_b32 v106, v107
	ds_read_b32 v107, v108
	ds_read_b32 v108, v109
	ds_read_b32 v109, v110
	ds_read_b32 v110, v111
	ds_read_b32 v111, v112
	ds_read_b32 v112, v113
	ds_read_b32 v113, v114
	s_waitcnt vmcnt(11) lgkmcnt(14)
	v_pk_fma_f32 v[8:9], v[28:29], v[62:63], v[8:9] op_sel_hi:[0,1,1]
	v_pk_fma_f32 v[10:11], v[28:29], v[64:65], v[10:11] op_sel_hi:[0,1,1]
	s_waitcnt vmcnt(10)
	v_pk_fma_f32 v[8:9], v[30:31], v[66:67], v[8:9] op_sel_hi:[0,1,1]
	v_pk_fma_f32 v[10:11], v[30:31], v[68:69], v[10:11] op_sel_hi:[0,1,1]
	s_addk_i32 s12, 0x100
	v_add_u32_e32 v19, 64, v19
	s_cmpk_eq_i32 s12, 0x200
	s_waitcnt vmcnt(9)
	v_pk_fma_f32 v[8:9], v[32:33], v[70:71], v[8:9] op_sel_hi:[0,1,1]
	v_pk_fma_f32 v[10:11], v[32:33], v[72:73], v[10:11] op_sel_hi:[0,1,1]
	s_waitcnt vmcnt(8)
	v_pk_fma_f32 v[8:9], v[34:35], v[74:75], v[8:9] op_sel_hi:[0,1,1]
	v_pk_fma_f32 v[10:11], v[34:35], v[76:77], v[10:11] op_sel_hi:[0,1,1]
	s_waitcnt vmcnt(7)
	v_pk_fma_f32 v[8:9], v[36:37], v[78:79], v[8:9] op_sel_hi:[0,1,1]
	v_pk_fma_f32 v[10:11], v[36:37], v[80:81], v[10:11] op_sel_hi:[0,1,1]
	s_waitcnt vmcnt(6)
	v_pk_fma_f32 v[8:9], v[38:39], v[82:83], v[8:9] op_sel_hi:[0,1,1]
	v_pk_fma_f32 v[10:11], v[38:39], v[84:85], v[10:11] op_sel_hi:[0,1,1]
	s_waitcnt vmcnt(5)
	v_pk_fma_f32 v[8:9], v[40:41], v[86:87], v[8:9] op_sel_hi:[0,1,1]
	v_pk_fma_f32 v[10:11], v[40:41], v[88:89], v[10:11] op_sel_hi:[0,1,1]
	s_waitcnt vmcnt(4)
	v_pk_fma_f32 v[8:9], v[42:43], v[90:91], v[8:9] op_sel_hi:[0,1,1]
	v_pk_fma_f32 v[10:11], v[42:43], v[92:93], v[10:11] op_sel_hi:[0,1,1]
	s_waitcnt vmcnt(3)
	v_pk_fma_f32 v[8:9], v[44:45], v[94:95], v[8:9] op_sel_hi:[0,1,1]
	v_pk_fma_f32 v[10:11], v[44:45], v[96:97], v[10:11] op_sel_hi:[0,1,1]
	s_waitcnt vmcnt(2)
	v_pk_fma_f32 v[8:9], v[46:47], v[98:99], v[8:9] op_sel_hi:[0,1,1]
	s_waitcnt lgkmcnt(12)
	v_pk_fma_f32 v[10:11], v[46:47], v[100:101], v[10:11] op_sel_hi:[0,1,1]
	s_waitcnt vmcnt(1) lgkmcnt(10)
	v_pk_fma_f32 v[8:9], v[48:49], v[102:103], v[8:9] op_sel_hi:[0,1,1]
	s_waitcnt lgkmcnt(8)
	v_pk_fma_f32 v[10:11], v[48:49], v[104:105], v[10:11] op_sel_hi:[0,1,1]
	s_waitcnt vmcnt(0) lgkmcnt(6)
	v_pk_fma_f32 v[8:9], v[20:21], v[106:107], v[8:9] op_sel_hi:[0,1,1]
	s_waitcnt lgkmcnt(4)
	v_pk_fma_f32 v[10:11], v[20:21], v[108:109], v[10:11] op_sel_hi:[0,1,1]
	s_waitcnt lgkmcnt(2)
	v_pk_fma_f32 v[8:9], v[12:13], v[110:111], v[8:9] op_sel_hi:[0,1,1]
	s_waitcnt lgkmcnt(0)
	v_pk_fma_f32 v[10:11], v[12:13], v[112:113], v[10:11] op_sel_hi:[0,1,1]
	s_cbranch_scc0 .LBB0_19
	ds_bpermute_b32 v6, v1, v8
	ds_bpermute_b32 v7, v1, v9
	ds_bpermute_b32 v12, v1, v10
	ds_bpermute_b32 v13, v1, v11
	s_waitcnt lgkmcnt(3)
	v_add_f32_e32 v6, v8, v6
	s_waitcnt lgkmcnt(2)
	v_add_f32_e32 v7, v9, v7
	s_waitcnt lgkmcnt(1)
	v_add_f32_e32 v8, v10, v12
	s_waitcnt lgkmcnt(0)
	v_add_f32_e32 v10, v11, v13
	ds_bpermute_b32 v9, v3, v6
	ds_bpermute_b32 v11, v3, v7
	ds_bpermute_b32 v12, v3, v8
	ds_bpermute_b32 v13, v3, v10
	s_and_saveexec_b64 s[12:13], vcc
	s_cbranch_execz .LBB0_22
	s_waitcnt lgkmcnt(2)
	v_add_f32_e32 v7, v7, v11
	v_add_f32_e32 v6, v6, v9
	s_waitcnt lgkmcnt(0)
	v_add_f32_e32 v10, v10, v13
	v_add_f32_e32 v8, v8, v12
	ds_write2_b32 v16, v6, v7 offset1:16
	ds_write2_b32 v16, v8, v10 offset0:32 offset1:48

; #define GAS __attribute__((address_space(1)))
; __device__ __forceinline__ float bf_lo(unsigned w) { return __uint_as_float(w << 16); }
; __device__ __forceinline__ float bf_hi(unsigned w) { return __uint_as_float(w & 0xffff0000u); }
; __device__ __forceinline__ void final_rows(Frame& F, const bf16* XA, const bf16* YS, const int* posi, const float* wl, const float* PART, const LAS int* tab, const float* gate, const float* g, float* out) {
;     ...
; #pragma unroll 2
;         for (int r = 0; r < 8; ++r) {
;             const int row = row0 + r;
;             const GAS unsigned long long* xr = (const GAS unsigned long long*)(XA + (size_t)row * D) + lane;
;             const int d0 = __builtin_amdgcn_readfirstlane(posi[2 * row]), d1 = __builtin_amdgcn_readfirstlane(posi[2 * row + 1]);
;             const float w0 = __builtin_bit_cast(float, __builtin_amdgcn_readfirstlane(__builtin_bit_cast(int, wl[d0]))), w1 = __builtin_bit_cast(float, __builtin_amdgcn_readfirstlane(__builtin_bit_cast(int, wl[d1])));
;             const int c0 = __builtin_amdgcn_readfirstlane(tab[d0 >> 14]) * 256 + (d0 & (ECAP - 1)), c1 = __builtin_amdgcn_readfirstlane(tab[d1 >> 14]) * 256 + (d1 & (ECAP - 1));
;             f32x4 ys[4];
;     ...
;             f32x4 v[4]; float s = 0.f;
; #pragma unroll
;             for (int j = 0; j < 4; ++j) { const unsigned long long xq = xr[64 * j]; const unsigned xl = (unsigned)xq, xh = (unsigned)(xq >> 32);
;                 v[j] = (f32x4){bf_lo(xl), bf_hi(xl), bf_lo(xh), bf_hi(xh)} + gt[j] * ys[j]; s += (v[j].x * v[j].x + v[j].y * v[j].y) + (v[j].z * v[j].z + v[j].w * v[j].w); }
;             const float rstd = rsqrtf(wave_sum(s) * (1.f / D) + RMS_EPS);
;             GAS f32x4* o = (GAS f32x4*)(out + (size_t)row * D) + lane;
; #pragma unroll
;             for (int j = 0; j < 4; ++j) o[64 * j] = v[j] * rstd * gf[j];
.LBB0_1948:
	s_ashr_i32 s3, s2, 31
	s_lshl_b64 s[4:5], s[2:3], 11
	s_add_i32 s26, s26, 2
	s_lshl_b64 s[2:3], s[2:3], 12
	s_cmp_eq_u32 s26, 8
	v_lshlrev_b32_e32 v12, 16, v194
	v_and_b32_e32 v13, 0xffff0000, v194
	v_lshlrev_b32_e32 v14, 16, v195
	v_and_b32_e32 v15, 0xffff0000, v195
	v_lshlrev_b32_e32 v70, 16, v196
	v_and_b32_e32 v71, 0xffff0000, v196
	v_lshlrev_b32_e32 v64, 16, v197
	v_and_b32_e32 v65, 0xffff0000, v197
	v_lshlrev_b32_e32 v72, 16, v198
	v_and_b32_e32 v73, 0xffff0000, v198
	v_lshlrev_b32_e32 v66, 16, v199
	v_and_b32_e32 v67, 0xffff0000, v199
	v_lshlrev_b32_e32 v76, 16, v200
	v_and_b32_e32 v77, 0xffff0000, v200
	v_lshlrev_b32_e32 v68, 16, v201
	v_and_b32_e32 v69, 0xffff0000, v201
	v_pk_fma_f32 v[0:1], v[16:17], v[0:1], v[12:13]
	v_pk_fma_f32 v[2:3], v[18:19], v[2:3], v[14:15]
	v_pk_fma_f32 v[4:5], v[20:21], v[4:5], v[70:71]
	v_pk_fma_f32 v[6:7], v[22:23], v[6:7], v[64:65]
	v_pk_fma_f32 v[10:11], v[34:35], v[10:11], v[66:67]
	v_pk_fma_f32 v[12:13], v[38:39], v[50:51], v[68:69]
	v_pk_fma_f32 v[14:15], v[36:37], v[48:49], v[76:77]
	v_pk_mul_f32 v[48:49], v[2:3], v[2:3]
	v_pk_mul_f32 v[50:51], v[0:1], v[0:1]
	v_pk_mul_f32 v[64:65], v[6:7], v[6:7]
	v_pk_mul_f32 v[66:67], v[4:5], v[4:5]
	v_pk_fma_f32 v[8:9], v[32:33], v[8:9], v[72:73]
	v_pk_mov_b32 v[72:73], v[50:51], v[48:49] op_sel:[1,0]
	v_mov_b32_e32 v51, v49
	v_pk_mov_b32 v[48:49], v[66:67], v[64:65] op_sel:[1,0]
	v_mov_b32_e32 v67, v65
	v_mul_f32_e32 v71, v14, v14
	v_mul_f32_e32 v68, v9, v9
	v_mul_f32_e32 v70, v11, v11
	v_pk_add_f32 v[50:51], v[72:73], v[50:51]
	v_pk_add_f32 v[48:49], v[48:49], v[66:67]
	v_mul_f32_e32 v74, v15, v15
	v_mul_f32_e32 v76, v12, v12
	v_mul_f32_e32 v77, v13, v13
	v_pk_fma_f32 v[64:65], v[8:9], v[8:9], v[68:69] op_sel_hi:[1,1,0]
	v_pk_fma_f32 v[68:69], v[10:11], v[10:11], v[70:71] op_sel_hi:[1,1,0]
	v_pk_add_f32 v[50:51], v[50:51], v[50:51] op_sel:[0,1] op_sel_hi:[1,0]
	v_pk_add_f32 v[48:49], v[48:49], v[48:49] op_sel:[0,1] op_sel_hi:[1,0]
	v_mov_b32_e32 v65, v76
	v_mov_b32_e32 v69, v77
	v_mov_b32_e32 v51, v71
	v_mov_b32_e32 v49, v74
	v_pk_add_f32 v[64:65], v[64:65], v[68:69]
	v_pk_add_f32 v[48:49], v[50:51], v[48:49]
	s_nop 0
	v_pk_add_f32 v[48:49], v[48:49], v[64:65]
	s_nop 0
	v_add_f32_e32 v48, v48, v49
	ds_bpermute_b32 v49, v75, v48
	s_waitcnt lgkmcnt(0)
	v_add_f32_e32 v48, v48, v49
	ds_bpermute_b32 v49, v78, v48
	s_waitcnt lgkmcnt(0)
	v_add_f32_e32 v48, v48, v49
	ds_bpermute_b32 v49, v79, v48
	s_waitcnt lgkmcnt(0)
	v_add_f32_e32 v48, v48, v49
	ds_bpermute_b32 v49, v80, v48
	s_waitcnt lgkmcnt(0)
	v_add_f32_e32 v48, v48, v49
	ds_bpermute_b32 v49, v81, v48
	s_waitcnt lgkmcnt(0)
	v_add_f32_e32 v48, v48, v49
	ds_bpermute_b32 v49, v82, v48
	s_waitcnt lgkmcnt(0)
	v_add_f32_e32 v48, v48, v49
	v_fmamk_f32 v48, v48, 0x3a800000, v85
	v_mul_f32_e32 v49, 0x4b800000, v48
	v_cmp_gt_f32_e32 vcc, s19, v48
	s_nop 1
	v_cndmask_b32_e32 v48, v48, v49, vcc
	v_rsq_f32_e32 v50, v48
	v_lshl_add_u64 v[48:49], v[60:61], 0, s[2:3]
	v_mul_f32_e32 v51, 0x45800000, v50
	v_cndmask_b32_e32 v50, v50, v51, vcc
	v_pk_mul_f32 v[0:1], v[0:1], v[50:51] op_sel_hi:[1,0]
	v_pk_mul_f32 v[2:3], v[2:3], v[50:51] op_sel_hi:[1,0]
	v_pk_mul_f32 v[4:5], v[4:5], v[50:51] op_sel_hi:[1,0]
	v_pk_mul_f32 v[6:7], v[6:7], v[50:51] op_sel_hi:[1,0]
	v_pk_mul_f32 v[8:9], v[8:9], v[50:51] op_sel_hi:[1,0]
	v_pk_mul_f32 v[10:11], v[10:11], v[50:51] op_sel_hi:[1,0]
	v_pk_mul_f32 v[64:65], v[14:15], v[50:51] op_sel_hi:[1,0]
	v_pk_mul_f32 v[12:13], v[12:13], v[50:51] op_sel_hi:[1,0]
	v_pk_mul_f32 v[2:3], v[26:27], v[2:3]
	v_pk_mul_f32 v[0:1], v[24:25], v[0:1]
	v_pk_mul_f32 v[6:7], v[30:31], v[6:7]
	v_pk_mul_f32 v[4:5], v[28:29], v[4:5]
	v_pk_mul_f32 v[10:11], v[42:43], v[10:11]
	v_pk_mul_f32 v[8:9], v[40:41], v[8:9]
	v_pk_mul_f32 v[14:15], v[46:47], v[12:13]
	v_pk_mul_f32 v[12:13], v[44:45], v[64:65]
	global_store_dwordx4 v[48:49], v[0:3], off nt
	global_store_dwordx4 v[48:49], v[4:7], off offset:1024 nt
	global_store_dwordx4 v[48:49], v[8:11], off offset:2048 nt
	global_store_dwordx4 v[48:49], v[12:15], off offset:3072 nt
	v_mov_b32_e32 v202, v206
	v_mov_b32_e32 v203, v207
	v_mov_b32_e32 v204, v208
	v_mov_b32_e32 v205, v209
	s_cbranch_scc1 .LBB0_1946
.LBB0_1949:
	s_add_i32 s4, s26, s25
	s_add_u32 s34, s34, 16
	s_addc_u32 s35, s35, 0
	global_load_dwordx4 v[206:209], v84, s[34:35]
	s_ashr_i32 s5, s4, 31
	s_lshl_b64 s[36:37], s[4:5], 11
	v_lshl_add_u64 v[214:215], v[54:55], 0, s[36:37]
	global_load_dwordx2 v[186:187], v[214:215], off nt
	global_load_dwordx2 v[188:189], v[214:215], off offset:512 nt
	global_load_dwordx2 v[190:191], v[214:215], off offset:1024 nt
	global_load_dwordx2 v[192:193], v[214:215], off offset:1536 nt
	global_load_dwordx2 v[194:195], v[214:215], off offset:2048 nt
	global_load_dwordx2 v[196:197], v[214:215], off offset:2560 nt
	global_load_dwordx2 v[198:199], v[214:215], off offset:3072 nt
	global_load_dwordx2 v[200:201], v[214:215], off offset:3584 nt
	v_readfirstlane_b32 s38, v204
	v_readfirstlane_b32 s39, v205
	s_mov_b32 s40, s38
	s_ashr_i32 s41, s38, 31
	s_lshl_b64 s[40:41], s[40:41], 2
	s_add_u32 s40, s22, s40
	s_addc_u32 s41, s23, s41
	s_mov_b32 s42, s39
	s_ashr_i32 s43, s39, 31
	s_lshl_b64 s[42:43], s[42:43], 2
	s_add_u32 s42, s22, s42
	s_addc_u32 s43, s23, s43
	global_load_dword v212, v84, s[40:41]
	global_load_dword v213, v84, s[42:43]
	v_readfirstlane_b32 s2, v202
	s_ashr_i32 s3, s2, 31
	s_lshl_b64 s[10:11], s[2:3], 2
	v_readfirstlane_b32 s8, v203
	s_add_u32 s10, s22, s10
	s_addc_u32 s11, s23, s11
	s_ashr_i32 s9, s8, 31
	s_lshl_b64 s[12:13], s[8:9], 2
	s_add_u32 s12, s22, s12
	s_addc_u32 s13, s23, s13
	global_load_dword v0, v84, s[10:11]
	global_load_dword v1, v84, s[12:13]
	s_ashr_i32 s0, s2, 14
	s_ashr_i32 s3, s8, 14
	s_lshl_b32 s0, s0, 2
	s_lshl_b32 s3, s3, 2
	s_add_i32 s0, s18, s0
	s_add_i32 s3, s18, s3
	v_mov_b32_e32 v2, s0
	v_mov_b32_e32 v3, s3
	ds_read_b32 v2, v2
	ds_read_b32 v3, v3
	s_and_b32 s0, s2, 0x3fff
	s_and_b32 s2, s8, 0x3fff
	s_mov_b64 s[12:13], -1
	s_waitcnt lgkmcnt(1)
	v_readfirstlane_b32 s3, v2
	s_waitcnt lgkmcnt(0)
	v_readfirstlane_b32 s5, v3
	s_lshl_b32 s3, s3, 8
	s_lshl_b32 s5, s5, 8
	s_add_i32 s10, s3, s0
	s_add_i32 s8, s5, s2
	s_max_i32 s0, s10, s8
	s_cmp_lt_i32 s0, 0x8000
	s_waitcnt vmcnt(1)
	v_readfirstlane_b32 s2, v0
	s_waitcnt vmcnt(0)
	v_readfirstlane_b32 s6, v1
	s_cbranch_scc1 .LBB0_1957
	v_mov_b32_e32 v48, 0
	v_mov_b32_e32 v49, v48
	v_mov_b32_e32 v50, v48
	v_mov_b32_e32 v51, v48
	v_mov_b32_e32 v0, v48
	v_mov_b32_e32 v1, v48
	v_mov_b32_e32 v64, v48
	v_mov_b32_e32 v65, v48
	v_mov_b32_e32 v66, v48
	v_mov_b32_e32 v67, v48
	v_mov_b32_e32 v68, v48
	v_mov_b32_e32 v69, v48
	v_mov_b32_e32 v70, v48
	v_mov_b32_e32 v71, v48
	v_mov_b32_e32 v72, v48
	v_mov_b32_e32 v73, v48

; #define GAS __attribute__((address_space(1)))
; __device__ __forceinline__ float bf_lo(unsigned w) { return __uint_as_float(w << 16); }
; __device__ __forceinline__ float bf_hi(unsigned w) { return __uint_as_float(w & 0xffff0000u); }
; __device__ __forceinline__ void final_rows(Frame& F, const bf16* XA, const bf16* YS, const int* posi, const float* wl, const float* PART, const LAS int* tab, const float* gate, const float* g, float* out) {
;     ...
;                 for (int sl = 0; sl < 2; ++sl) { const int cc = sl ? c1 : c0; const float ww = sl ? w1 : w0;
;                     if (cc < pg8::TAIL_M0 * 256) { const GAS unsigned long long* y0 = (const GAS unsigned long long*)(YS + (size_t)cc * D) + lane;
; #pragma unroll
;                         for (int j = 0; j < 4; ++j) { const unsigned long long a = y0[64 * j]; const unsigned al = (unsigned)a, ah = (unsigned)(a >> 32); ys[j] += (f32x4){bf_lo(al), bf_hi(al), bf_lo(ah), bf_hi(ah)} * ww; } }
.LBB0_1953:
	s_andn2_b64 vcc, exec, s[16:17]
	s_cbranch_vccnz .LBB0_1955
	s_ashr_i32 s15, s14, 31
	s_lshl_b64 s[14:15], s[14:15], 11
	v_lshl_add_u64 v[0:1], v[58:59], 0, s[14:15]
	global_load_dwordx2 v[2:3], v[0:1], off nt
	global_load_dwordx2 v[4:5], v[0:1], off offset:512 nt
	global_load_dwordx2 v[6:7], v[0:1], off offset:1024 nt
	global_load_dwordx2 v[8:9], v[0:1], off offset:1536 nt
	s_waitcnt vmcnt(3)
	v_lshlrev_b32_e32 v0, 16, v2
	v_and_b32_e32 v1, 0xffff0000, v2
	v_lshlrev_b32_e32 v2, 16, v3
	v_and_b32_e32 v3, 0xffff0000, v3
	s_waitcnt vmcnt(2)
	v_lshlrev_b32_e32 v10, 16, v4
	v_and_b32_e32 v11, 0xffff0000, v4
	v_lshlrev_b32_e32 v4, 16, v5
	v_and_b32_e32 v5, 0xffff0000, v5
	s_waitcnt vmcnt(1)
	v_lshlrev_b32_e32 v12, 16, v6
	v_and_b32_e32 v13, 0xffff0000, v6
	v_lshlrev_b32_e32 v14, 16, v7
	v_and_b32_e32 v15, 0xffff0000, v7
	s_waitcnt vmcnt(0)
	v_lshlrev_b32_e32 v86, 16, v8
	v_and_b32_e32 v87, 0xffff0000, v8
	v_lshlrev_b32_e32 v88, 16, v9
	v_and_b32_e32 v89, 0xffff0000, v9
	v_pk_fma_f32 v[2:3], v[74:75], v[2:3], v[64:65] op_sel_hi:[0,1,1]
	v_pk_fma_f32 v[0:1], v[74:75], v[0:1], v[76:77] op_sel_hi:[0,1,1]
	v_pk_fma_f32 v[6:7], v[74:75], v[4:5], v[68:69] op_sel_hi:[0,1,1]
	v_pk_fma_f32 v[4:5], v[74:75], v[10:11], v[66:67] op_sel_hi:[0,1,1]
	v_pk_fma_f32 v[10:11], v[74:75], v[14:15], v[72:73] op_sel_hi:[0,1,1]
	v_pk_fma_f32 v[8:9], v[74:75], v[12:13], v[70:71] op_sel_hi:[0,1,1]
	v_pk_mul_f32 v[14:15], v[74:75], v[88:89] op_sel_hi:[0,1]
	v_pk_mul_f32 v[12:13], v[74:75], v[86:87] op_sel_hi:[0,1]

; #define GAS __attribute__((address_space(1)))
; __device__ __forceinline__ float bf_lo(unsigned w) { return __uint_as_float(w << 16); }
; __device__ __forceinline__ float bf_hi(unsigned w) { return __uint_as_float(w & 0xffff0000u); }
; __device__ __forceinline__ void final_rows(Frame& F, const bf16* XA, const bf16* YS, const int* posi, const float* wl, const float* PART, const LAS int* tab, const float* gate, const float* g, float* out) {
;     ...
;             if (c0 < pg8::TAIL_M0 * 256 && c1 < pg8::TAIL_M0 * 256) {
;                 const GAS unsigned long long* y0 = (const GAS unsigned long long*)(YS + (size_t)c0 * D) + lane; const GAS unsigned long long* y1 = (const GAS unsigned long long*)(YS + (size_t)c1 * D) + lane;
; #pragma unroll
;                 for (int j = 0; j < 4; ++j) { const unsigned long long a = y0[64 * j], c = y1[64 * j]; const unsigned al = (unsigned)a, ah = (unsigned)(a >> 32), cl = (unsigned)c, ch = (unsigned)(c >> 32);
;                     ys[j] = (f32x4){bf_lo(al), bf_hi(al), bf_lo(ah), bf_hi(ah)} * w0 + (f32x4){bf_lo(cl), bf_hi(cl), bf_lo(ch), bf_hi(ch)} * w1; }
.LBB0_1957:
	s_and_b64 vcc, exec, s[12:13]
	s_cbranch_vccz .LBB0_1959
	s_ashr_i32 s11, s10, 31
	s_ashr_i32 s9, s8, 31
	s_lshl_b64 s[10:11], s[10:11], 11
	s_lshl_b64 s[8:9], s[8:9], 11
	v_lshl_add_u64 v[0:1], v[58:59], 0, s[10:11]
	v_lshl_add_u64 v[4:5], v[58:59], 0, s[8:9]
	global_load_dwordx2 v[2:3], v[0:1], off nt
	global_load_dwordx2 v[6:7], v[4:5], off nt
	global_load_dwordx2 v[8:9], v[0:1], off offset:512 nt
	global_load_dwordx2 v[10:11], v[4:5], off offset:512 nt
	global_load_dwordx2 v[12:13], v[0:1], off offset:1024 nt
	global_load_dwordx2 v[14:15], v[4:5], off offset:1024 nt
	global_load_dwordx2 v[48:49], v[0:1], off offset:1536 nt
	global_load_dwordx2 v[50:51], v[4:5], off offset:1536 nt
	s_waitcnt vmcnt(6)
	v_lshlrev_b32_e32 v4, 16, v6
	v_and_b32_e32 v5, 0xffff0000, v6
	v_lshlrev_b32_e32 v6, 16, v7
	v_and_b32_e32 v7, 0xffff0000, v7
	s_waitcnt vmcnt(4)
	v_lshlrev_b32_e32 v66, 16, v10
	v_and_b32_e32 v67, 0xffff0000, v10
	v_lshlrev_b32_e32 v10, 16, v11
	v_and_b32_e32 v11, 0xffff0000, v11
	s_waitcnt vmcnt(2)
	v_lshlrev_b32_e32 v70, 16, v14
	v_and_b32_e32 v71, 0xffff0000, v14
	v_lshlrev_b32_e32 v14, 16, v15
	v_and_b32_e32 v15, 0xffff0000, v15
	s_waitcnt vmcnt(0)
	v_lshlrev_b32_e32 v76, 16, v50
	v_and_b32_e32 v77, 0xffff0000, v50
	v_lshlrev_b32_e32 v50, 16, v51
	v_and_b32_e32 v51, 0xffff0000, v51
	v_lshlrev_b32_e32 v0, 16, v2
	v_and_b32_e32 v1, 0xffff0000, v2
	v_lshlrev_b32_e32 v2, 16, v3
	v_and_b32_e32 v3, 0xffff0000, v3
	v_lshlrev_b32_e32 v64, 16, v8
	v_and_b32_e32 v65, 0xffff0000, v8
	v_lshlrev_b32_e32 v8, 16, v9
	v_and_b32_e32 v9, 0xffff0000, v9
	v_lshlrev_b32_e32 v68, 16, v12
	v_and_b32_e32 v69, 0xffff0000, v12
	v_lshlrev_b32_e32 v12, 16, v13
	v_and_b32_e32 v13, 0xffff0000, v13
	v_lshlrev_b32_e32 v72, 16, v48
	v_and_b32_e32 v73, 0xffff0000, v48
	v_lshlrev_b32_e32 v48, 16, v49
	v_and_b32_e32 v49, 0xffff0000, v49
	v_pk_mul_f32 v[4:5], s[6:7], v[4:5] op_sel_hi:[0,1]
	v_pk_mul_f32 v[6:7], s[6:7], v[6:7] op_sel_hi:[0,1]
	v_pk_mul_f32 v[66:67], s[6:7], v[66:67] op_sel_hi:[0,1]
	v_pk_mul_f32 v[10:11], s[6:7], v[10:11] op_sel_hi:[0,1]
	v_pk_mul_f32 v[70:71], s[6:7], v[70:71] op_sel_hi:[0,1]
	v_pk_mul_f32 v[14:15], s[6:7], v[14:15] op_sel_hi:[0,1]
	v_pk_mul_f32 v[76:77], s[6:7], v[76:77] op_sel_hi:[0,1]
	v_pk_mul_f32 v[50:51], s[6:7], v[50:51] op_sel_hi:[0,1]
	v_pk_fma_f32 v[2:3], s[2:3], v[2:3], v[6:7] op_sel_hi:[0,1,1]
	v_pk_fma_f32 v[0:1], s[2:3], v[0:1], v[4:5] op_sel_hi:[0,1,1]
	v_pk_fma_f32 v[6:7], s[2:3], v[8:9], v[10:11] op_sel_hi:[0,1,1]
	v_pk_fma_f32 v[4:5], s[2:3], v[64:65], v[66:67] op_sel_hi:[0,1,1]
	v_pk_fma_f32 v[10:11], s[2:3], v[12:13], v[14:15] op_sel_hi:[0,1,1]
	v_pk_fma_f32 v[8:9], s[2:3], v[68:69], v[70:71] op_sel_hi:[0,1,1]
	v_pk_fma_f32 v[50:51], s[2:3], v[48:49], v[50:51] op_sel_hi:[0,1,1]
	v_pk_fma_f32 v[48:49], s[2:3], v[72:73], v[76:77] op_sel_hi:[0,1,1]
; #define GAS __attribute__((address_space(1)))
; __device__ __forceinline__ float bf_lo(unsigned w) { return __uint_as_float(w << 16); }
; __device__ __forceinline__ float bf_hi(unsigned w) { return __uint_as_float(w & 0xffff0000u); }
; __device__ __forceinline__ void final_rows(Frame& F, const bf16* XA, const bf16* YS, const int* posi, const float* wl, const float* PART, const LAS int* tab, const float* gate, const float* g, float* out) {
;     ...
;             const int row = row0 + r;
;             const GAS unsigned long long* xr = (const GAS unsigned long long*)(XA + (size_t)row * D) + lane;
;             const int d0 = __builtin_amdgcn_readfirstlane(posi[2 * row]), d1 = __builtin_amdgcn_readfirstlane(posi[2 * row + 1]);
;             const float w0 = __builtin_bit_cast(float, __builtin_amdgcn_readfirstlane(__builtin_bit_cast(int, wl[d0]))), w1 = __builtin_bit_cast(float, __builtin_amdgcn_readfirstlane(__builtin_bit_cast(int, wl[d1])));
;             const int c0 = __builtin_amdgcn_readfirstlane(tab[d0 >> 14]) * 256 + (d0 & (ECAP - 1)), c1 = __builtin_amdgcn_readfirstlane(tab[d1 >> 14]) * 256 + (d1 & (ECAP - 1));
;             f32x4 ys[4];
;             if (c0 < pg8::TAIL_M0 * 256 && c1 < pg8::TAIL_M0 * 256) {
;     ...
;             f32x4 v[4]; float s = 0.f;
; #pragma unroll
;             for (int j = 0; j < 4; ++j) { const unsigned long long xq = xr[64 * j]; const unsigned xl = (unsigned)xq, xh = (unsigned)(xq >> 32);
;                 v[j] = (f32x4){bf_lo(xl), bf_hi(xl), bf_lo(xh), bf_hi(xh)} + gt[j] * ys[j]; s += (v[j].x * v[j].x + v[j].y * v[j].y) + (v[j].z * v[j].z + v[j].w * v[j].w); }
;             const float rstd = rsqrtf(wave_sum(s) * (1.f / D) + RMS_EPS);
;             GAS f32x4* o = (GAS f32x4*)(out + (size_t)row * D) + lane;
; #pragma unroll
;             for (int j = 0; j < 4; ++j) o[64 * j] = v[j] * rstd * gf[j];
.LBB0_1959:
	s_ashr_i32 s5, s4, 31
	s_lshl_b64 s[2:3], s[4:5], 11
	s_add_i32 s2, s4, 1
	s_lshl_b32 s8, s2, 1
	s_lshl_b64 s[4:5], s[4:5], 12
	s_ashr_i32 s9, s8, 31
	v_lshlrev_b32_e32 v12, 16, v186
	v_and_b32_e32 v13, 0xffff0000, v186
	v_lshlrev_b32_e32 v14, 16, v187
	v_and_b32_e32 v15, 0xffff0000, v187
	v_lshlrev_b32_e32 v70, 16, v188
	v_and_b32_e32 v71, 0xffff0000, v188
	v_lshlrev_b32_e32 v64, 16, v189
	v_and_b32_e32 v65, 0xffff0000, v189
	v_lshlrev_b32_e32 v72, 16, v190
	v_and_b32_e32 v73, 0xffff0000, v190
	v_lshlrev_b32_e32 v66, 16, v191
	v_and_b32_e32 v67, 0xffff0000, v191
	v_lshlrev_b32_e32 v76, 16, v192
	v_and_b32_e32 v77, 0xffff0000, v192
	v_lshlrev_b32_e32 v68, 16, v193
	v_and_b32_e32 v69, 0xffff0000, v193
	v_pk_fma_f32 v[0:1], v[16:17], v[0:1], v[12:13]
	v_pk_fma_f32 v[2:3], v[18:19], v[2:3], v[14:15]
	v_pk_fma_f32 v[4:5], v[20:21], v[4:5], v[70:71]
	v_pk_fma_f32 v[6:7], v[22:23], v[6:7], v[64:65]
	v_pk_fma_f32 v[10:11], v[34:35], v[10:11], v[66:67]
	v_pk_fma_f32 v[12:13], v[38:39], v[50:51], v[68:69]
	v_pk_fma_f32 v[14:15], v[36:37], v[48:49], v[76:77]
	v_pk_mul_f32 v[48:49], v[2:3], v[2:3]
	v_pk_mul_f32 v[50:51], v[0:1], v[0:1]
	v_pk_mul_f32 v[64:65], v[6:7], v[6:7]
	v_pk_mul_f32 v[66:67], v[4:5], v[4:5]
	v_pk_fma_f32 v[8:9], v[32:33], v[8:9], v[72:73]
	v_pk_mov_b32 v[72:73], v[50:51], v[48:49] op_sel:[1,0]
	v_mov_b32_e32 v51, v49
	v_pk_mov_b32 v[48:49], v[66:67], v[64:65] op_sel:[1,0]
	v_mov_b32_e32 v67, v65
	v_mul_f32_e32 v71, v14, v14
	v_mul_f32_e32 v68, v9, v9
	v_mul_f32_e32 v70, v11, v11
	v_pk_add_f32 v[50:51], v[72:73], v[50:51]
	v_pk_add_f32 v[48:49], v[48:49], v[66:67]
	v_mul_f32_e32 v74, v15, v15
	v_mul_f32_e32 v76, v12, v12
	v_mul_f32_e32 v77, v13, v13
	v_pk_fma_f32 v[64:65], v[8:9], v[8:9], v[68:69] op_sel_hi:[1,1,0]
	v_pk_fma_f32 v[68:69], v[10:11], v[10:11], v[70:71] op_sel_hi:[1,1,0]
	v_pk_add_f32 v[50:51], v[50:51], v[50:51] op_sel:[0,1] op_sel_hi:[1,0]
	v_pk_add_f32 v[48:49], v[48:49], v[48:49] op_sel:[0,1] op_sel_hi:[1,0]
	v_mov_b32_e32 v65, v76
	v_mov_b32_e32 v69, v77
	v_mov_b32_e32 v51, v71
	v_mov_b32_e32 v49, v74
	v_pk_add_f32 v[64:65], v[64:65], v[68:69]
	v_pk_add_f32 v[48:49], v[50:51], v[48:49]
	s_nop 0
	v_pk_add_f32 v[48:49], v[48:49], v[64:65]
	s_nop 0
	v_add_f32_e32 v48, v48, v49
	ds_bpermute_b32 v49, v75, v48
	s_waitcnt lgkmcnt(0)
	v_add_f32_e32 v48, v48, v49
	ds_bpermute_b32 v49, v78, v48
	s_waitcnt lgkmcnt(0)
	v_add_f32_e32 v48, v48, v49
	ds_bpermute_b32 v49, v79, v48
	s_waitcnt lgkmcnt(0)
	v_add_f32_e32 v48, v48, v49
	ds_bpermute_b32 v49, v80, v48
	s_waitcnt lgkmcnt(0)
	v_add_f32_e32 v48, v48, v49
	ds_bpermute_b32 v49, v81, v48
	s_waitcnt lgkmcnt(0)
	v_add_f32_e32 v50, v48, v49
	ds_bpermute_b32 v51, v82, v50
	v_lshl_add_u64 v[48:49], v[60:61], 0, s[4:5]
	s_lshl_b64 s[4:5], s[8:9], 2
	s_add_u32 s4, s20, s4
	s_addc_u32 s5, s21, s5
	s_waitcnt lgkmcnt(0)
	v_add_f32_e32 v50, v50, v51
	v_fmamk_f32 v50, v50, 0x3a800000, v85
	v_mul_f32_e32 v51, 0x4b800000, v50
	v_cmp_gt_f32_e32 vcc, s19, v50
	s_nop 1
	v_cndmask_b32_e32 v50, v50, v51, vcc
	v_rsq_f32_e32 v50, v50
	s_nop 0
	v_mul_f32_e32 v51, 0x45800000, v50
	v_cndmask_b32_e32 v50, v50, v51, vcc
	v_pk_mul_f32 v[0:1], v[0:1], v[50:51] op_sel_hi:[1,0]
	v_pk_mul_f32 v[2:3], v[2:3], v[50:51] op_sel_hi:[1,0]
	v_pk_mul_f32 v[4:5], v[4:5], v[50:51] op_sel_hi:[1,0]
	v_pk_mul_f32 v[6:7], v[6:7], v[50:51] op_sel_hi:[1,0]
	v_pk_mul_f32 v[8:9], v[8:9], v[50:51] op_sel_hi:[1,0]
	v_pk_mul_f32 v[10:11], v[10:11], v[50:51] op_sel_hi:[1,0]
	v_pk_mul_f32 v[64:65], v[14:15], v[50:51] op_sel_hi:[1,0]
	v_pk_mul_f32 v[12:13], v[12:13], v[50:51] op_sel_hi:[1,0]
	v_pk_mul_f32 v[2:3], v[26:27], v[2:3]
	v_pk_mul_f32 v[0:1], v[24:25], v[0:1]
	v_pk_mul_f32 v[6:7], v[30:31], v[6:7]
	v_pk_mul_f32 v[4:5], v[28:29], v[4:5]
	v_pk_mul_f32 v[10:11], v[42:43], v[10:11]
	v_pk_mul_f32 v[8:9], v[40:41], v[8:9]
	v_pk_mul_f32 v[14:15], v[46:47], v[12:13]
	v_pk_mul_f32 v[12:13], v[44:45], v[64:65]
	global_store_dwordx4 v[48:49], v[0:3], off nt
	global_store_dwordx4 v[48:49], v[4:7], off offset:1024 nt
	global_store_dwordx4 v[48:49], v[8:11], off offset:2048 nt
	global_store_dwordx4 v[48:49], v[12:15], off offset:3072 nt
	v_readfirstlane_b32 s4, v204
	s_ashr_i32 s5, s4, 31
	s_lshl_b64 s[10:11], s[4:5], 2
	v_readfirstlane_b32 s8, v205
	s_add_u32 s10, s22, s10
	s_addc_u32 s11, s23, s11
	s_ashr_i32 s9, s8, 31
	s_lshl_b64 s[12:13], s[8:9], 2
	s_add_u32 s12, s22, s12
	s_addc_u32 s13, s23, s13
	s_ashr_i32 s0, s4, 14
	s_ashr_i32 s3, s8, 14
	s_lshl_b32 s0, s0, 2
	s_lshl_b32 s3, s3, 2
	s_add_i32 s0, s18, s0
	s_add_i32 s3, s18, s3
	v_mov_b32_e32 v2, s0
	v_mov_b32_e32 v3, s3
	ds_read_b32 v2, v2
	ds_read_b32 v3, v3
	s_and_b32 s0, s4, 0x3fff
	s_and_b32 s3, s8, 0x3fff
	s_mov_b64 s[12:13], -1
	s_waitcnt lgkmcnt(1)
	v_readfirstlane_b32 s4, v2
	s_waitcnt lgkmcnt(0)
	v_readfirstlane_b32 s5, v3
	s_lshl_b32 s4, s4, 8
	s_lshl_b32 s5, s5, 8
	s_add_i32 s10, s4, s0
	s_add_i32 s8, s5, s3
	s_max_i32 s0, s10, s8
	s_cmp_lt_i32 s0, 0x8000
	v_readfirstlane_b32 s4, v212
	v_readfirstlane_b32 s6, v213
	s_cbranch_scc1 .LBB0_1967
	v_mov_b32_e32 v48, 0
	v_mov_b32_e32 v49, v48
	v_mov_b32_e32 v50, v48
	v_mov_b32_e32 v51, v48
	v_mov_b32_e32 v0, v48
	v_mov_b32_e32 v1, v48
	v_mov_b32_e32 v64, v48
	v_mov_b32_e32 v65, v48
	v_mov_b32_e32 v66, v48
	v_mov_b32_e32 v67, v48
	v_mov_b32_e32 v68, v48
	v_mov_b32_e32 v69, v48
	v_mov_b32_e32 v70, v48
	v_mov_b32_e32 v71, v48
	v_mov_b32_e32 v72, v48
	v_mov_b32_e32 v73, v48

; #define GAS __attribute__((address_space(1)))
; __device__ __forceinline__ float bf_lo(unsigned w) { return __uint_as_float(w << 16); }
; __device__ __forceinline__ float bf_hi(unsigned w) { return __uint_as_float(w & 0xffff0000u); }
; __device__ __forceinline__ void final_rows(Frame& F, const bf16* XA, const bf16* YS, const int* posi, const float* wl, const float* PART, const LAS int* tab, const float* gate, const float* g, float* out) {
;     ...
;             if (c0 < pg8::TAIL_M0 * 256 && c1 < pg8::TAIL_M0 * 256) {
;                 const GAS unsigned long long* y0 = (const GAS unsigned long long*)(YS + (size_t)c0 * D) + lane; const GAS unsigned long long* y1 = (const GAS unsigned long long*)(YS + (size_t)c1 * D) + lane;
; #pragma unroll
;                 for (int j = 0; j < 4; ++j) { const unsigned long long a = y0[64 * j], c = y1[64 * j]; const unsigned al = (unsigned)a, ah = (unsigned)(a >> 32), cl = (unsigned)c, ch = (unsigned)(c >> 32);
;                     ys[j] = (f32x4){bf_lo(al), bf_hi(al), bf_lo(ah), bf_hi(ah)} * w0 + (f32x4){bf_lo(cl), bf_hi(cl), bf_lo(ch), bf_hi(ch)} * w1; }
.LBB0_1967:
	s_and_b64 vcc, exec, s[12:13]
	s_cbranch_vccz .LBB0_1948
	s_ashr_i32 s11, s10, 31
	s_ashr_i32 s9, s8, 31
	s_lshl_b64 s[10:11], s[10:11], 11
	s_lshl_b64 s[8:9], s[8:9], 11
	v_lshl_add_u64 v[0:1], v[58:59], 0, s[10:11]
	v_lshl_add_u64 v[4:5], v[58:59], 0, s[8:9]
	global_load_dwordx2 v[2:3], v[0:1], off nt
	global_load_dwordx2 v[6:7], v[4:5], off nt
	global_load_dwordx2 v[8:9], v[0:1], off offset:512 nt
	global_load_dwordx2 v[10:11], v[4:5], off offset:512 nt
	global_load_dwordx2 v[12:13], v[0:1], off offset:1024 nt
	global_load_dwordx2 v[14:15], v[4:5], off offset:1024 nt
	global_load_dwordx2 v[48:49], v[0:1], off offset:1536 nt
	global_load_dwordx2 v[50:51], v[4:5], off offset:1536 nt
	s_waitcnt vmcnt(6)
	v_lshlrev_b32_e32 v4, 16, v6
	v_and_b32_e32 v5, 0xffff0000, v6
	v_lshlrev_b32_e32 v6, 16, v7
	v_and_b32_e32 v7, 0xffff0000, v7
	s_waitcnt vmcnt(4)
	v_lshlrev_b32_e32 v66, 16, v10
	v_and_b32_e32 v67, 0xffff0000, v10
	v_lshlrev_b32_e32 v10, 16, v11
	v_and_b32_e32 v11, 0xffff0000, v11
	s_waitcnt vmcnt(2)
	v_lshlrev_b32_e32 v70, 16, v14
	v_and_b32_e32 v71, 0xffff0000, v14
	v_lshlrev_b32_e32 v14, 16, v15
	v_and_b32_e32 v15, 0xffff0000, v15
	s_waitcnt vmcnt(0)
	v_lshlrev_b32_e32 v76, 16, v50
	v_and_b32_e32 v77, 0xffff0000, v50
	v_lshlrev_b32_e32 v50, 16, v51
	v_and_b32_e32 v51, 0xffff0000, v51
	v_lshlrev_b32_e32 v0, 16, v2
	v_and_b32_e32 v1, 0xffff0000, v2
	v_lshlrev_b32_e32 v2, 16, v3
	v_and_b32_e32 v3, 0xffff0000, v3
	v_lshlrev_b32_e32 v64, 16, v8
	v_and_b32_e32 v65, 0xffff0000, v8
	v_lshlrev_b32_e32 v8, 16, v9
	v_and_b32_e32 v9, 0xffff0000, v9
	v_lshlrev_b32_e32 v68, 16, v12
	v_and_b32_e32 v69, 0xffff0000, v12
	v_lshlrev_b32_e32 v12, 16, v13
	v_and_b32_e32 v13, 0xffff0000, v13
	v_lshlrev_b32_e32 v72, 16, v48
	v_and_b32_e32 v73, 0xffff0000, v48
	v_lshlrev_b32_e32 v48, 16, v49
	v_and_b32_e32 v49, 0xffff0000, v49
	v_pk_mul_f32 v[4:5], s[6:7], v[4:5] op_sel_hi:[0,1]
	v_pk_mul_f32 v[6:7], s[6:7], v[6:7] op_sel_hi:[0,1]
	v_pk_mul_f32 v[66:67], s[6:7], v[66:67] op_sel_hi:[0,1]
	v_pk_mul_f32 v[10:11], s[6:7], v[10:11] op_sel_hi:[0,1]
	v_pk_mul_f32 v[70:71], s[6:7], v[70:71] op_sel_hi:[0,1]
	v_pk_mul_f32 v[14:15], s[6:7], v[14:15] op_sel_hi:[0,1]
	v_pk_mul_f32 v[76:77], s[6:7], v[76:77] op_sel_hi:[0,1]
	v_pk_mul_f32 v[50:51], s[6:7], v[50:51] op_sel_hi:[0,1]
	v_pk_fma_f32 v[2:3], s[4:5], v[2:3], v[6:7] op_sel_hi:[0,1,1]
	v_pk_fma_f32 v[0:1], s[4:5], v[0:1], v[4:5] op_sel_hi:[0,1,1]
	v_pk_fma_f32 v[6:7], s[4:5], v[8:9], v[10:11] op_sel_hi:[0,1,1]
	v_pk_fma_f32 v[4:5], s[4:5], v[64:65], v[66:67] op_sel_hi:[0,1,1]
	v_pk_fma_f32 v[10:11], s[4:5], v[12:13], v[14:15] op_sel_hi:[0,1,1]
	v_pk_fma_f32 v[8:9], s[4:5], v[68:69], v[70:71] op_sel_hi:[0,1,1]
	v_pk_fma_f32 v[50:51], s[4:5], v[48:49], v[50:51] op_sel_hi:[0,1,1]
	v_pk_fma_f32 v[48:49], s[4:5], v[72:73], v[76:77] op_sel_hi:[0,1,1]
	s_branch .LBB0_1948
